# v032 + 9.8% of the MoE weight conversion deferred out of the prologue into the workgroups that idle during the two top-k phases (P5: 192 WGs, P14: 224 WGs; 2 items per wave)
# speedup vs baseline: 1.0089x; 1.0031x over previous
; #define LAS __attribute__((address_space(3)))
; __device__ __forceinline__ int tidx() { int t = threadIdx.x; asm volatile("" : "+v"(t)); return t; }
; __device__ __forceinline__ void phase_cvt_moe(LAS unsigned char* lds, const CvtMoe a) {
;     const int tid_ = tidx(), wave = tid_ >> 6, lane = tid_ & 63;
;     LAS float* scr = (LAS float*)(lds + wave * CVT_SCR);
;     const int gw = blockIdx.x * 8 + wave, NGW = gridDim.x * 8;
;     constexpr int IG = (D / 64) * (FF / 64), ID = (FF / 64) * (D / 64);
;     for (int it = gw; it < 2 * NE * (2 * IG + ID); it += NGW) {
;         const int e = it / (2 * IG + ID); int r = it % (2 * IG + ID);
;         if (r < 2 * IG) { const int up = r / IG; r %= IG; const int nblk = FF / 64, kb = r / nblk, nb = r % nblk, n0 = nb * 64;
;             cvt_item((up ? a.wu : a.wg) + (size_t)e * D * FF, D, FF, a.gu + (size_t)e * 2 * FF * D, (n0 / 128) * 256 + up * 128 + (n0 % 128), kb * 64, n0, scr, lane); }
;         else { r -= 2 * IG; const int nblk = D / 64, kb = r / nblk, nb = r % nblk; cvt_item(a.wd + (size_t)e * FF * D, FF, D, a.dn + (size_t)e * D * FF, nb * 64, kb * 64, nb * 64, scr, lane); }
;     }
.LBB0_55:
	s_or_b64 exec, exec, s[4:5]
	s_add_u32 s4, s90, 0x30a13600
	s_addc_u32 s5, s91, 0
	v_writelane_b32 v250, s4, 6
	v_mov_b32_e32 v4, v0
	s_nop 0
	v_writelane_b32 v250, s5, 7
	s_add_u32 s4, s90, 0x46a13600
	s_addc_u32 s5, s91, 0
	v_writelane_b32 v250, s4, 8
	v_ashrrev_i32_e32 v2, 6, v4
	v_add_u32_e32 v5, s14, v2
	v_writelane_b32 v250, s5, 9
	s_mov_b32 s4, 0xee00
	v_cmp_gt_i32_e32 vcc, s4, v5
	s_and_saveexec_b64 s[4:5], vcc
	s_cbranch_execz .LBB0_62
	s_movk_i32 s6, 0x4100
	v_mul_lo_u32 v3, v2, s6
	v_add_u32_e32 v8, 0, v3
	v_lshlrev_b32_e32 v3, 2, v4
	v_bfe_u32 v6, v4, 4, 2
	v_and_b32_e32 v44, 60, v3
	v_bfe_u32 v7, v4, 3, 3
	v_lshlrev_b32_e32 v4, 3, v4
	v_lshl_add_u32 v20, v44, 2, v8
	v_mul_u32_u24_e32 v21, 0x104, v6
	v_and_b32_e32 v4, 56, v4
	v_mul_u32_u24_e32 v9, 0x104, v4
	v_lshlrev_b32_e32 v10, 2, v7
	v_lshlrev_b32_e32 v16, 2, v2
	v_add_u32_e32 v20, v20, v21
	v_mov_b32_e32 v3, 0
	v_add3_u32 v8, v8, v9, v10
	v_or_b32_e32 v9, 8, v7
	v_or_b32_e32 v10, 16, v7
	v_or_b32_e32 v11, 24, v7
	v_or_b32_e32 v12, 32, v7
	v_or_b32_e32 v13, 40, v7
	v_or_b32_e32 v14, 48, v7
	v_or_b32_e32 v15, 56, v7
	v_lshl_add_u32 v16, s2, 5, v16
	v_lshlrev_b32_e32 v17, 2, v1
	v_lshl_add_u32 v18, v2, 6, s3
	v_lshlrev_b32_e32 v19, 6, v1
	s_mov_b64 s[6:7], 0
	s_mov_b32 s3, 0x3e0f83e1
	s_movk_i32 s10, 0x57f
	s_mov_b32 s11, 0xb00000
	v_add_u32_e32 v21, 0x410, v20
	v_add_u32_e32 v22, 0x418, v20
	v_add_u32_e32 v23, 0x820, v20
	v_add_u32_e32 v24, 0x828, v20
	v_add_u32_e32 v25, 0xc30, v20
	v_add_u32_e32 v26, 0xc38, v20
	v_add_u32_e32 v27, 0x1040, v20
	v_add_u32_e32 v28, 0x1048, v20
	v_add_u32_e32 v29, 0x1450, v20
	v_add_u32_e32 v30, 0x1458, v20
	v_add_u32_e32 v31, 0x1860, v20
	v_add_u32_e32 v32, 0x1868, v20
	v_add_u32_e32 v33, 0x1c70, v20
	v_add_u32_e32 v34, 0x1c78, v20
	v_add_u32_e32 v35, 0x2080, v20
	v_add_u32_e32 v36, 0x2088, v20
	v_add_u32_e32 v37, 0x2490, v20
	v_add_u32_e32 v38, 0x2498, v20
	v_add_u32_e32 v39, 0x28a0, v20
	v_add_u32_e32 v40, 0x28a8, v20
	v_add_u32_e32 v41, 0x2cb0, v20
	v_add_u32_e32 v42, 0x2cb8, v20
	s_movk_i32 s12, 0xba3
	s_mov_b32 s13, 0xb000
	s_mov_b32 s14, 0x16000
	s_mov_b32 s15, 0x21000
	s_mov_b32 s16, 0x2c000
	s_mov_b32 s17, 0x37000
	s_mov_b32 s18, 0x42000
	s_mov_b32 s19, 0x4d000
	s_mov_b32 s20, 0x58000
	s_mov_b32 s21, 0x63000
	s_mov_b32 s22, 0x6e000
	s_mov_b32 s23, 0x79000
	s_mov_b32 s24, 0x84000
	s_mov_b32 s25, 0x8f000
	s_mov_b32 s26, 0x9a000
	s_mov_b32 s27, 0xa5000
	s_mov_b32 s28, 0xedff
	v_lshlrev_b32_e32 v2, 2, v44
	v_add_u32_e32 v43, 0x30c0, v20
	v_add_u32_e32 v44, 0x30c8, v20
	v_add_u32_e32 v45, 0x34d0, v20
	v_add_u32_e32 v46, 0x34d8, v20
	v_mov_b32_e32 v47, 6
	v_mov_b32_e32 v48, 1
	v_mov_b32_e32 v49, 8
	v_mov_b32_e32 v50, 7
	s_branch .LBB0_58

; #define LAS __attribute__((address_space(3)))
; __device__ __forceinline__ int tidx() { int t = threadIdx.x; asm volatile("" : "+v"(t)); return t; }
; __device__ __forceinline__ void phase_cvt_moe(LAS unsigned char* lds, const CvtMoe a) {
;     const int tid_ = tidx(), wave = tid_ >> 6, lane = tid_ & 63;
;     LAS float* scr = (LAS float*)(lds + wave * CVT_SCR);
;     const int gw = blockIdx.x * 8 + wave, NGW = gridDim.x * 8;
;     constexpr int IG = (D / 64) * (FF / 64), ID = (FF / 64) * (D / 64);
;     for (int it = gw; it < 2 * NE * (2 * IG + ID); it += NGW) {
;         const int e = it / (2 * IG + ID); int r = it % (2 * IG + ID);
;         if (r < 2 * IG) { const int up = r / IG; r %= IG; const int nblk = FF / 64, kb = r / nblk, nb = r % nblk, n0 = nb * 64;
; __device__ __forceinline__ void ph_topk(const int vc, const Params& p, LAS unsigned char* lds, bool with_ctx) {
;     ...
;             if (b == 0) { const int from = with_ctx ? 2 * CAPL + 2 * CAPC : 2 * CAPL;
;                 for (int m = from + tidx(); m < MEXP; m += NTHR) { WSP(int, OFF_RIDX)[e * MEXP + m] = 0; WSP(float, OFF_GATE)[e * MEXP + m] = 0.f; } }
.LBB0_935:
	v_add_co_u32_e32 v8, vcc, 0xfffdc000, v2
	v_add_u32_e32 v4, 0x200, v4
	s_movk_i32 s8, 0x6ff
	v_addc_co_u32_e32 v9, vcc, -1, v3, vcc
	s_mov_b64 s[6:7], 0x800
	v_cmp_lt_i32_e32 vcc, s8, v4
	global_store_dword v[2:3], v7, off
	v_lshl_add_u64 v[2:3], v[2:3], 0, s[6:7]
	s_or_b64 s[4:5], vcc, s[4:5]
	global_store_dword v[8:9], v7, off
	s_andn2_b64 exec, exec, s[4:5]
	s_cbranch_execnz .LBB0_935
	s_branch .LBB0_697
	s_branch .LBB0_936
.Lcvp5_entry:
	s_sub_i32 s0, s94, 64
	v_readlane_b32 s2, v250, 26
	v_readlane_b32 s3, v250, 27
	s_nop 3
	s_sub_u32 s2, s2, 0xc0
	s_subb_u32 s3, s3, 0
	s_load_dwordx2 s[38:39], s[2:3], 0x90
	s_load_dwordx2 s[40:41], s[2:3], 0x98
	s_load_dwordx2 s[34:35], s[2:3], 0xa0
	s_lshl_b32 s0, s0, 3
	s_add_i32 s0, s0, 0xee00
	v_mov_b32_e32 v131, 0x600
	s_waitcnt lgkmcnt(0)
	s_add_u32 s4, s90, 0x30a13600
	s_addc_u32 s5, s91, 0
	v_writelane_b32 v250, s4, 6
	v_mov_b32_e32 v130, v0
	s_nop 0
	v_writelane_b32 v250, s5, 7
	s_add_u32 s4, s90, 0x46a13600
	s_addc_u32 s5, s91, 0
	v_writelane_b32 v250, s4, 8
	v_ashrrev_i32_e32 v2, 6, v130
	v_add_u32_e32 v5, s0, v2
	v_writelane_b32 v250, s5, 9
	s_mov_b32 s4, 0xfa00
	v_cmp_gt_i32_e32 vcc, s4, v5
	s_and_saveexec_b64 s[4:5], vcc
	s_cbranch_execz .Lcvp5_62
	s_movk_i32 s6, 0x4100
	v_mul_lo_u32 v3, v2, s6
	v_add_u32_e32 v8, 0, v3
	v_lshlrev_b32_e32 v3, 2, v130
	v_bfe_u32 v6, v130, 4, 2
	v_and_b32_e32 v44, 60, v3
	v_bfe_u32 v7, v130, 3, 3
	v_lshlrev_b32_e32 v130, 3, v130
	v_lshl_add_u32 v20, v44, 2, v8
	v_mul_u32_u24_e32 v21, 0x104, v6
	v_and_b32_e32 v130, 56, v130
	v_mul_u32_u24_e32 v9, 0x104, v130
	v_lshlrev_b32_e32 v10, 2, v7
	v_lshlrev_b32_e32 v16, 2, v2
	v_add_u32_e32 v20, v20, v21
	v_mov_b32_e32 v3, 0
	v_add3_u32 v8, v8, v9, v10
	v_or_b32_e32 v9, 8, v7
	v_or_b32_e32 v10, 16, v7
	v_or_b32_e32 v11, 24, v7
	v_or_b32_e32 v12, 32, v7
	v_or_b32_e32 v13, 40, v7
	v_or_b32_e32 v14, 48, v7
	v_or_b32_e32 v15, 56, v7
	v_lshlrev_b32_e32 v16, 2, v5
	v_lshlrev_b32_e32 v17, 2, v131
	v_lshlrev_b32_e32 v18, 6, v5
	v_lshlrev_b32_e32 v19, 6, v131
	s_mov_b64 s[6:7], 0
	s_mov_b32 s3, 0x3e0f83e1
	s_movk_i32 s10, 0x57f
	s_mov_b32 s11, 0xb00000
	v_add_u32_e32 v21, 0x410, v20
	v_add_u32_e32 v22, 0x418, v20
	v_add_u32_e32 v23, 0x820, v20
	v_add_u32_e32 v24, 0x828, v20
	v_add_u32_e32 v25, 0xc30, v20
	v_add_u32_e32 v26, 0xc38, v20
	v_add_u32_e32 v27, 0x1040, v20
	v_add_u32_e32 v28, 0x1048, v20
	v_add_u32_e32 v29, 0x1450, v20
	v_add_u32_e32 v30, 0x1458, v20
	v_add_u32_e32 v31, 0x1860, v20
	v_add_u32_e32 v32, 0x1868, v20
	v_add_u32_e32 v33, 0x1c70, v20
	v_add_u32_e32 v34, 0x1c78, v20
	v_add_u32_e32 v35, 0x2080, v20
	v_add_u32_e32 v36, 0x2088, v20
	v_add_u32_e32 v37, 0x2490, v20
	v_add_u32_e32 v38, 0x2498, v20
	v_add_u32_e32 v39, 0x28a0, v20
	v_add_u32_e32 v40, 0x28a8, v20
	v_add_u32_e32 v41, 0x2cb0, v20
	v_add_u32_e32 v42, 0x2cb8, v20
	s_movk_i32 s64, 0xba3
	s_mov_b32 s65, 0xb000
	s_mov_b32 s66, 0x16000
	s_mov_b32 s67, 0x21000
	s_mov_b32 s16, 0x2c000
	s_mov_b32 s68, 0x37000
	s_mov_b32 s69, 0x42000
	s_mov_b32 s19, 0x4d000
	s_mov_b32 s20, 0x58000
	s_mov_b32 s21, 0x63000
	s_mov_b32 s70, 0x6e000
	s_mov_b32 s23, 0x79000
	s_mov_b32 s24, 0x84000
	s_mov_b32 s25, 0x8f000
	s_mov_b32 s26, 0x9a000
	s_mov_b32 s27, 0xa5000
	s_mov_b32 s71, 0xf9ff
	v_lshlrev_b32_e32 v2, 2, v44
	v_add_u32_e32 v43, 0x30c0, v20
	v_add_u32_e32 v44, 0x30c8, v20
	v_add_u32_e32 v45, 0x34d0, v20
	v_add_u32_e32 v46, 0x34d8, v20
	v_mov_b32_e32 v47, 6
	v_mov_b32_e32 v132, 1
	v_mov_b32_e32 v133, 8
	v_mov_b32_e32 v134, 7
	s_branch .Lcvp5_58

; #define LAS __attribute__((address_space(3)))
; __device__ __forceinline__ void cvt_item(const float* W, int K, int N, bf16_t* WT, int drow0, int k0, int n0, LAS float* scr, int lane) {
;     f32x4 v[16];
;     const int lr = lane >> 4, lc4 = (lane & 15) * 4;
; #pragma unroll
;     for (int i = 0; i < 16; ++i) v[i] = __builtin_nontemporal_load((const f32x4*)(W + (size_t)(k0 + 4 * i + lr) * N + n0 + lc4));
; #pragma unroll
;     for (int i = 0; i < 16; ++i) { LAS float* d = scr + (4 * i + lr) * 65 + lc4; d[0] = v[i][0]; d[1] = v[i][1]; d[2] = v[i][2]; d[3] = v[i][3]; }
; __device__ __forceinline__ void phase_cvt_moe(LAS unsigned char* lds, const CvtMoe a) {
;     ...
;     for (int it = gw; it < 2 * NE * (2 * IG + ID); it += NGW) {
;         const int e = it / (2 * IG + ID); int r = it % (2 * IG + ID);
;         if (r < 2 * IG) { const int up = r / IG; r %= IG; const int nblk = FF / 64, kb = r / nblk, nb = r % nblk, n0 = nb * 64;
;             cvt_item((up ? a.wu : a.wg) + (size_t)e * D * FF, D, FF, a.gu + (size_t)e * 2 * FF * D, (n0 / 128) * 256 + up * 128 + (n0 % 128), kb * 64, n0, scr, lane); }
;         else { r -= 2 * IG; const int nblk = D / 64, kb = r / nblk, nb = r % nblk; cvt_item(a.wd + (size_t)e * FF * D, FF, D, a.dn + (size_t)e * D * FF, nb * 64, kb * 64, nb * 64, scr, lane); }
.Lcvp5_58:
	v_mul_hi_i32 v135, v5, s3
	v_lshrrev_b32_e32 v136, 31, v135
	v_ashrrev_i32_e32 v135, 9, v135
	v_add_u32_e32 v135, v135, v136
	v_mul_i32_i24_e32 v137, 0x840, v135
	v_sub_u32_e32 v136, v5, v137
	v_cmp_lt_i32_e32 vcc, s10, v136
	s_and_saveexec_b64 s[8:9], vcc
	s_xor_b64 s[8:9], exec, s[8:9]
	s_cbranch_execz .Lcvp5_60
	v_lshlrev_b32_e32 v136, 6, v137
	v_sub_u32_e32 v118, v18, v136
	v_lshlrev_b32_e32 v136, 2, v137
	v_sub_u32_e32 v136, v16, v136
	v_and_b32_e32 v136, 0x7fffffc0, v136
	v_mov_b64_e32 v[138:139], s[34:35]
	v_and_b32_e32 v119, 0x3c0, v118
	v_add_u32_e32 v120, 0xffffea00, v136
	v_mad_i64_i32 v[138:139], s[72:73], v135, s11, v[138:139]
	v_or_b32_e32 v112, v120, v6
	v_lshlrev_b32_e32 v136, 2, v119
	v_mov_b32_e32 v137, v3
	v_lshl_add_u64 v[136:137], v[138:139], 0, v[136:137]
	v_mov_b32_e32 v113, v3
	v_or_b32_e32 v138, 4, v112
	v_mov_b32_e32 v139, v3
	v_or_b32_e32 v144, 8, v112
	v_mov_b32_e32 v145, v3
	v_or_b32_e32 v146, 12, v112
	v_mov_b32_e32 v147, v3
	v_or_b32_e32 v68, 16, v112
	v_mov_b32_e32 v69, v3
	v_or_b32_e32 v70, 20, v112
	v_mov_b32_e32 v71, v3
	v_or_b32_e32 v76, 24, v112
	v_mov_b32_e32 v77, v3
	v_or_b32_e32 v78, 28, v112
	v_mov_b32_e32 v79, v3
	v_or_b32_e32 v84, 32, v112
	v_mov_b32_e32 v85, v3
	v_or_b32_e32 v86, 36, v112
	v_mov_b32_e32 v87, v3
	v_or_b32_e32 v92, 40, v112
	v_mov_b32_e32 v93, v3
	v_or_b32_e32 v94, 44, v112
	v_mov_b32_e32 v95, v3
	v_or_b32_e32 v100, 48, v112
	v_mov_b32_e32 v101, v3
	v_or_b32_e32 v102, 52, v112
	v_mov_b32_e32 v103, v3
	v_or_b32_e32 v108, 56, v112
	v_mov_b32_e32 v109, v3
	v_lshl_add_u64 v[114:115], v[136:137], 0, v[2:3]
	v_lshlrev_b64 v[136:137], 12, v[112:113]
	v_lshlrev_b64 v[138:139], 12, v[138:139]
	v_lshlrev_b64 v[144:145], 12, v[144:145]
	v_lshlrev_b64 v[146:147], 12, v[146:147]
	v_lshlrev_b64 v[68:69], 12, v[68:69]
	v_lshlrev_b64 v[70:71], 12, v[70:71]
	v_lshlrev_b64 v[76:77], 12, v[76:77]
	v_lshlrev_b64 v[78:79], 12, v[78:79]
	v_lshlrev_b64 v[84:85], 12, v[84:85]
	v_lshlrev_b64 v[86:87], 12, v[86:87]
	v_lshlrev_b64 v[92:93], 12, v[92:93]
	v_lshlrev_b64 v[94:95], 12, v[94:95]
	v_lshlrev_b64 v[100:101], 12, v[100:101]
	v_lshlrev_b64 v[102:103], 12, v[102:103]
	v_lshlrev_b64 v[108:109], 12, v[108:109]
	v_lshl_add_u64 v[136:137], v[114:115], 0, v[136:137]
	v_lshl_add_u64 v[140:141], v[114:115], 0, v[138:139]
	v_lshl_add_u64 v[144:145], v[114:115], 0, v[144:145]
	v_lshl_add_u64 v[64:65], v[114:115], 0, v[146:147]
	v_lshl_add_u64 v[68:69], v[114:115], 0, v[68:69]
	v_lshl_add_u64 v[72:73], v[114:115], 0, v[70:71]
	v_lshl_add_u64 v[76:77], v[114:115], 0, v[76:77]
	v_lshl_add_u64 v[80:81], v[114:115], 0, v[78:79]
	v_lshl_add_u64 v[84:85], v[114:115], 0, v[84:85]
	v_lshl_add_u64 v[88:89], v[114:115], 0, v[86:87]
	v_lshl_add_u64 v[92:93], v[114:115], 0, v[92:93]
	v_lshl_add_u64 v[96:97], v[114:115], 0, v[94:95]
	v_lshl_add_u64 v[100:101], v[114:115], 0, v[100:101]
	v_lshl_add_u64 v[104:105], v[114:115], 0, v[102:103]
	v_lshl_add_u64 v[108:109], v[114:115], 0, v[108:109]
	v_or_b32_e32 v112, 60, v112
	global_load_dwordx4 v[136:139], v[136:137], off nt
	s_nop 0
	global_load_dwordx4 v[140:143], v[140:141], off nt
	s_nop 0
	global_load_dwordx4 v[144:147], v[144:145], off nt
	s_nop 0
	global_load_dwordx4 v[64:67], v[64:65], off nt
	s_nop 0
	global_load_dwordx4 v[68:71], v[68:69], off nt
	s_nop 0
	global_load_dwordx4 v[72:75], v[72:73], off nt
	s_nop 0
	global_load_dwordx4 v[76:79], v[76:77], off nt
	s_nop 0
	global_load_dwordx4 v[80:83], v[80:81], off nt
	s_nop 0
	global_load_dwordx4 v[84:87], v[84:85], off nt
	s_nop 0
	global_load_dwordx4 v[88:91], v[88:89], off nt
	s_nop 0
	global_load_dwordx4 v[92:95], v[92:93], off nt
	s_nop 0
	global_load_dwordx4 v[96:99], v[96:97], off nt
	s_nop 0
	global_load_dwordx4 v[100:103], v[100:101], off nt
	s_nop 0
	global_load_dwordx4 v[104:107], v[104:105], off nt
	v_lshlrev_b64 v[112:113], 12, v[112:113]
	global_load_dwordx4 v[108:111], v[108:109], off nt
	v_lshl_add_u64 v[112:113], v[114:115], 0, v[112:113]
	global_load_dwordx4 v[112:115], v[112:113], off nt
	v_mul_hi_i32_i24_e32 v117, 0x580000, v135
	v_mul_i32_i24_e32 v116, 0x580000, v135
	v_add_u32_e32 v135, 0x38e0, v20
	s_waitcnt vmcnt(15)
	ds_write2_b32 v20, v136, v137 offset1:1
	ds_write2_b32 v20, v138, v139 offset0:2 offset1:3
	s_waitcnt vmcnt(14)
	ds_write2_b32 v21, v140, v141 offset1:1
	ds_write2_b32 v22, v142, v143 offset1:1
	s_waitcnt vmcnt(13)
	ds_write2_b32 v23, v144, v145 offset1:1
	ds_write2_b32 v24, v146, v147 offset1:1
	s_waitcnt vmcnt(12)
	ds_write2_b32 v25, v64, v65 offset1:1
	ds_write2_b32 v26, v66, v67 offset1:1
	s_waitcnt vmcnt(11)
	ds_write2_b32 v27, v68, v69 offset1:1
	ds_write2_b32 v28, v70, v71 offset1:1
	s_waitcnt vmcnt(10)
	ds_write2_b32 v29, v72, v73 offset1:1
	ds_write2_b32 v30, v74, v75 offset1:1
	s_waitcnt vmcnt(9)
	ds_write2_b32 v31, v76, v77 offset1:1
	ds_write2_b32 v32, v78, v79 offset1:1
	s_waitcnt vmcnt(8)
	ds_write2_b32 v33, v80, v81 offset1:1
	ds_write2_b32 v34, v82, v83 offset1:1
	s_waitcnt vmcnt(7)
	ds_write2_b32 v35, v84, v85 offset1:1
	ds_write2_b32 v36, v86, v87 offset1:1
	s_waitcnt vmcnt(6)
	ds_write2_b32 v37, v88, v89 offset1:1
	ds_write2_b32 v38, v90, v91 offset1:1
	s_waitcnt vmcnt(5)
	ds_write2_b32 v39, v92, v93 offset1:1
	ds_write2_b32 v40, v94, v95 offset1:1
	s_waitcnt vmcnt(4)
	ds_write2_b32 v41, v96, v97 offset1:1
	ds_write2_b32 v42, v98, v99 offset1:1
	s_waitcnt vmcnt(3)
	ds_write2_b32 v43, v100, v101 offset1:1
	ds_write2_b32 v44, v102, v103 offset1:1
	s_waitcnt vmcnt(2)
	ds_write2_b32 v45, v104, v105 offset1:1
	ds_write2_b32 v46, v106, v107 offset1:1
	v_readlane_b32 s72, v250, 8
	s_waitcnt vmcnt(1)
; #define LAS __attribute__((address_space(3)))
; __device__ __forceinline__ unsigned cvt_pk_bf16(float lo, float hi) { const f32x2 v = {lo, hi}; const bf16v2_t r = __builtin_convertvector(v, bf16v2_t); return __builtin_bit_cast(unsigned, r); }
; __device__ __forceinline__ void cvt_item(const float* W, int K, int N, bf16_t* WT, int drow0, int k0, int n0, LAS float* scr, int lane) {
;     ...
;     for (int i = 0; i < 16; ++i) { LAS float* d = scr + (4 * i + lr) * 65 + lc4; d[0] = v[i][0]; d[1] = v[i][1]; d[2] = v[i][2]; d[3] = v[i][3]; }
;     asm volatile("s_waitcnt lgkmcnt(0)" ::: "memory");
;     const int c = lane & 7;
; #pragma unroll
;     for (int j = 0; j < 8; ++j) { const int n = (lane >> 3) + 8 * j; const LAS float* s = scr + (8 * c) * 65 + n;
;         u32x4 o; o.x = cvt_pk_bf16(s[0 * 65], s[1 * 65]); o.y = cvt_pk_bf16(s[2 * 65], s[3 * 65]); o.z = cvt_pk_bf16(s[4 * 65], s[5 * 65]); o.w = cvt_pk_bf16(s[6 * 65], s[7 * 65]);
;         __builtin_nontemporal_store(o, (u32x4*)(WT + ((size_t)((drow0 + n) >> 7) * (K >> 6) + (k0 >> 6)) * 8192 + ((drow0 + n) & 127) * 64 + 8 * c)); }
;     asm volatile("s_waitcnt lgkmcnt(0)" ::: "memory");
; }
	ds_write2_b32 v135, v108, v109 offset1:1
	v_add_u32_e32 v135, 0x38e8, v20
	ds_write2_b32 v135, v110, v111 offset1:1
	v_add_u32_e32 v135, 0x3cf0, v20
	s_waitcnt vmcnt(0)
	ds_write2_b32 v135, v112, v113 offset1:1
	v_add_u32_e32 v135, 0x3cf8, v20
	ds_write2_b32 v135, v114, v115 offset1:1
	s_waitcnt lgkmcnt(0)
	ds_read2_b32 v[140:141], v8 offset0:65 offset1:73
	ds_read2_b32 v[142:143], v8 offset1:8
	ds_read2_b32 v[144:145], v8 offset0:130 offset1:138
	ds_read2_b32 v[146:147], v8 offset0:195 offset1:203
	v_add_u32_e32 v135, 0x400, v8
	ds_read2_b32 v[64:65], v135 offset0:4 offset1:12
	ds_read2_b32 v[66:67], v135 offset0:69 offset1:77
	ds_read2_b32 v[68:69], v135 offset0:134 offset1:142
	ds_read2_b32 v[70:71], v135 offset0:199 offset1:207
	v_lshrrev_b32_e32 v72, 6, v120
	s_waitcnt lgkmcnt(6)
	v_cvt_pk_bf16_f32 v136, v142, v140
	v_bfe_u32 v142, v118, 7, 3
	v_readlane_b32 s73, v250, 9
	v_or_b32_e32 v140, v119, v7
	v_mad_u32_u24 v72, v142, 44, v72
	v_mov_b32_e32 v73, v3
	v_lshl_add_u64 v[116:117], s[72:73], 0, v[116:117]
	v_lshlrev_b64 v[72:73], 14, v[72:73]
	v_lshlrev_b32_e32 v140, 7, v140
	v_lshl_add_u64 v[72:73], v[116:117], 0, v[72:73]
	v_and_b32_e32 v74, 0x2380, v140
	v_mov_b32_e32 v75, v3
	v_lshl_add_u64 v[74:75], v[72:73], 0, v[74:75]
	v_lshlrev_b32_e32 v76, 1, v130
	v_mov_b32_e32 v77, v3
	v_or_b32_e32 v140, v119, v9
	s_waitcnt lgkmcnt(4)
	v_cvt_pk_bf16_f32 v137, v144, v146
	s_waitcnt lgkmcnt(2)
	v_cvt_pk_bf16_f32 v138, v64, v66
	s_waitcnt lgkmcnt(0)
	v_cvt_pk_bf16_f32 v139, v68, v70
	v_lshl_add_u64 v[74:75], v[74:75], 0, v[76:77]
	v_lshlrev_b32_e32 v140, 7, v140
	global_store_dwordx4 v[74:75], v[136:139], off nt
	v_and_b32_e32 v140, 0x2780, v140
	s_nop 0
	v_cvt_pk_bf16_f32 v136, v143, v141
	v_mov_b32_e32 v141, v3
	v_lshl_add_u64 v[140:141], v[72:73], 0, v[140:141]
	v_cvt_pk_bf16_f32 v137, v145, v147
	v_cvt_pk_bf16_f32 v138, v65, v67
	v_cvt_pk_bf16_f32 v139, v69, v71
	v_lshl_add_u64 v[140:141], v[140:141], 0, v[76:77]
	ds_read2_b32 v[142:143], v8 offset0:16 offset1:24
	ds_read2_b32 v[144:145], v8 offset0:81 offset1:89
	ds_read2_b32 v[146:147], v8 offset0:146 offset1:154
	ds_read2_b32 v[64:65], v8 offset0:211 offset1:219
	ds_read2_b32 v[66:67], v135 offset0:20 offset1:28
	ds_read2_b32 v[68:69], v135 offset0:85 offset1:93
	ds_read2_b32 v[70:71], v135 offset0:150 offset1:158
	ds_read2_b32 v[74:75], v135 offset0:215 offset1:223
	global_store_dwordx4 v[140:141], v[136:139], off nt
	v_or_b32_e32 v140, v119, v10
	v_lshlrev_b32_e32 v140, 7, v140
	v_and_b32_e32 v140, 0x2b80, v140
	v_mov_b32_e32 v141, v3
	v_lshl_add_u64 v[140:141], v[72:73], 0, v[140:141]
	s_waitcnt lgkmcnt(6)
	v_cvt_pk_bf16_f32 v136, v142, v144
	s_waitcnt lgkmcnt(4)
	v_cvt_pk_bf16_f32 v137, v146, v64
	s_waitcnt lgkmcnt(2)
	v_cvt_pk_bf16_f32 v138, v66, v68
	s_waitcnt lgkmcnt(0)
	v_cvt_pk_bf16_f32 v139, v70, v74
	v_lshl_add_u64 v[140:141], v[140:141], 0, v[76:77]
	global_store_dwordx4 v[140:141], v[136:139], off nt
	v_or_b32_e32 v140, v119, v11
	v_lshlrev_b32_e32 v140, 7, v140
	v_and_b32_e32 v140, 0x2f80, v140
	v_mov_b32_e32 v141, v3
	v_lshl_add_u64 v[140:141], v[72:73], 0, v[140:141]
	v_cvt_pk_bf16_f32 v136, v143, v145
	v_cvt_pk_bf16_f32 v137, v147, v65
	v_cvt_pk_bf16_f32 v138, v67, v69
	v_cvt_pk_bf16_f32 v139, v71, v75
	v_lshl_add_u64 v[140:141], v[140:141], 0, v[76:77]
	ds_read2_b32 v[142:143], v8 offset0:32 offset1:40
	ds_read2_b32 v[144:145], v8 offset0:97 offset1:105
	ds_read2_b32 v[146:147], v8 offset0:162 offset1:170
	ds_read2_b32 v[64:65], v8 offset0:227 offset1:235
	ds_read2_b32 v[66:67], v135 offset0:36 offset1:44
	ds_read2_b32 v[68:69], v135 offset0:101 offset1:109
	ds_read2_b32 v[70:71], v135 offset0:166 offset1:174
	ds_read2_b32 v[74:75], v135 offset0:231 offset1:239
	global_store_dwordx4 v[140:141], v[136:139], off nt
	v_or_b32_e32 v140, v119, v12
	v_lshlrev_b32_e32 v140, 7, v140
	v_and_b32_e32 v140, 0x3380, v140
	v_mov_b32_e32 v141, v3
	v_lshl_add_u64 v[140:141], v[72:73], 0, v[140:141]
	s_waitcnt lgkmcnt(6)
	v_cvt_pk_bf16_f32 v136, v142, v144
	s_waitcnt lgkmcnt(4)
	v_cvt_pk_bf16_f32 v137, v146, v64
	s_waitcnt lgkmcnt(2)
	v_cvt_pk_bf16_f32 v138, v66, v68
	s_waitcnt lgkmcnt(0)
	v_cvt_pk_bf16_f32 v139, v70, v74
	v_lshl_add_u64 v[140:141], v[140:141], 0, v[76:77]
	global_store_dwordx4 v[140:141], v[136:139], off nt
	v_or_b32_e32 v140, v119, v13
	v_lshlrev_b32_e32 v140, 7, v140
	v_cvt_pk_bf16_f32 v136, v143, v145
	v_cvt_pk_bf16_f32 v137, v147, v65
	v_cvt_pk_bf16_f32 v138, v67, v69
	v_cvt_pk_bf16_f32 v139, v71, v75
	v_and_b32_e32 v140, 0x3780, v140
	v_mov_b32_e32 v141, v3
	ds_read2_b32 v[142:143], v8 offset0:48 offset1:56
	ds_read2_b32 v[144:145], v8 offset0:113 offset1:121
	ds_read2_b32 v[146:147], v8 offset0:178 offset1:186
	ds_read2_b32 v[64:65], v8 offset0:243 offset1:251
	ds_read2_b32 v[66:67], v135 offset0:52 offset1:60
	ds_read2_b32 v[68:69], v135 offset0:117 offset1:125
	ds_read2_b32 v[70:71], v135 offset0:182 offset1:190
	ds_read2_b32 v[74:75], v135 offset0:247 offset1:255
	v_lshl_add_u64 v[140:141], v[72:73], 0, v[140:141]
	v_or_b32_e32 v135, v119, v14
	v_lshl_add_u64 v[140:141], v[140:141], 0, v[76:77]
	v_lshlrev_b32_e32 v135, 7, v135
	global_store_dwordx4 v[140:141], v[136:139], off nt
	v_and_b32_e32 v140, 0x3b80, v135
	v_mov_b32_e32 v141, v3
	v_lshl_add_u64 v[140:141], v[72:73], 0, v[140:141]
	v_or_b32_e32 v135, v119, v15
	s_waitcnt lgkmcnt(6)
	v_cvt_pk_bf16_f32 v136, v142, v144
	s_waitcnt lgkmcnt(4)
	v_cvt_pk_bf16_f32 v137, v146, v64
	s_waitcnt lgkmcnt(2)
	v_cvt_pk_bf16_f32 v138, v66, v68
	s_waitcnt lgkmcnt(0)
	v_cvt_pk_bf16_f32 v139, v70, v74
	v_lshl_add_u64 v[140:141], v[140:141], 0, v[76:77]
	v_lshlrev_b32_e32 v135, 7, v135
	global_store_dwordx4 v[140:141], v[136:139], off nt
	v_and_b32_e32 v140, 0x3f80, v135
	v_mov_b32_e32 v141, v3
	v_lshl_add_u64 v[140:141], v[72:73], 0, v[140:141]
	v_cvt_pk_bf16_f32 v136, v143, v145
	v_cvt_pk_bf16_f32 v137, v147, v65
	v_cvt_pk_bf16_f32 v138, v67, v69
	v_cvt_pk_bf16_f32 v139, v71, v75
	v_lshl_add_u64 v[140:141], v[140:141], 0, v[76:77]
	global_store_dwordx4 v[140:141], v[136:139], off nt
	s_waitcnt lgkmcnt(0)

; #define LAS __attribute__((address_space(3)))
; __device__ __forceinline__ int tidx() { int t = threadIdx.x; asm volatile("" : "+v"(t)); return t; }
; __device__ __forceinline__ void ph_topk(const int vc, const Params& p, LAS unsigned char* lds, bool with_ctx) {
;     const int nitems = with_ctx ? 64 : 32;
;     for (int it = vc; it < nitems; it += gridDim.x) {
;         if (it < 32) { const int b = it >> 4, e = it & 15;
;             topk_list<16>(p, lds, WSP(float, OFF_AFFL) + ((size_t)b * 16 + e) * SEQ, SEQ, CAPL, b * SEQ, b * CAPL, e);
;             if (b == 0) { const int from = with_ctx ? 2 * CAPL + 2 * CAPC : 2 * CAPL;
;                 for (int m = from + tidx(); m < MEXP; m += NTHR) { WSP(int, OFF_RIDX)[e * MEXP + m] = 0; WSP(float, OFF_GATE)[e * MEXP + m] = 0.f; } }
;         } else { const int q = it - 32, b = q >> 4, e = q & 15;
;             topk_list<1>(p, lds, WSP(float, OFF_AFFC) + ((size_t)b * 16 + e) * CTX, CTX, CAPC, ML + b * CTX, 2 * CAPL + b * CAPC, e); }
;     }
; }
.Lcvp5_62:
	s_or_b64 exec, exec, s[4:5]
	s_branch .LBB0_937
.LBB0_936:
	v_readlane_b32 s95, v250, 38
	v_readlane_b32 s94, v250, 34

; #define LAS __attribute__((address_space(3)))
; __device__ __forceinline__ int tidx() { int t = threadIdx.x; asm volatile("" : "+v"(t)); return t; }
; __device__ __forceinline__ void phase_cvt_moe(LAS unsigned char* lds, const CvtMoe a) {
;     const int tid_ = tidx(), wave = tid_ >> 6, lane = tid_ & 63;
;     LAS float* scr = (LAS float*)(lds + wave * CVT_SCR);
;     const int gw = blockIdx.x * 8 + wave, NGW = gridDim.x * 8;
;     constexpr int IG = (D / 64) * (FF / 64), ID = (FF / 64) * (D / 64);
;     for (int it = gw; it < 2 * NE * (2 * IG + ID); it += NGW) {
;         const int e = it / (2 * IG + ID); int r = it % (2 * IG + ID);
;         if (r < 2 * IG) { const int up = r / IG; r %= IG; const int nblk = FF / 64, kb = r / nblk, nb = r % nblk, n0 = nb * 64;
; __device__ __forceinline__ void ph_topk(const int vc, const Params& p, LAS unsigned char* lds, bool with_ctx) {
;     ...
;             if (b == 0) { const int from = with_ctx ? 2 * CAPL + 2 * CAPC : 2 * CAPL;
;                 for (int m = from + tidx(); m < MEXP; m += NTHR) { WSP(int, OFF_RIDX)[e * MEXP + m] = 0; WSP(float, OFF_GATE)[e * MEXP + m] = 0.f; } }
.LBB0_2270:
	v_add_co_u32_e32 v6, vcc, 0xfffdc000, v2
	v_add_u32_e32 v4, 0x200, v4
	s_movk_i32 s8, 0x6ff
	v_addc_co_u32_e32 v7, vcc, -1, v3, vcc
	s_mov_b64 s[6:7], 0x800
	v_cmp_lt_i32_e32 vcc, s8, v4
	global_store_dword v[2:3], v1, off
	v_lshl_add_u64 v[2:3], v[2:3], 0, s[6:7]
	s_or_b64 s[2:3], vcc, s[2:3]
	global_store_dword v[6:7], v1, off
	s_andn2_b64 exec, exec, s[2:3]
	s_cbranch_execnz .LBB0_2270
	s_branch .LBB0_2074
	s_branch .LBB0_2271
.Lcvp14_entry:
	s_sub_i32 s0, s94, 32
	v_readlane_b32 s2, v250, 26
	v_readlane_b32 s3, v250, 27
	s_nop 3
	s_sub_u32 s2, s2, 0xc0
	s_subb_u32 s3, s3, 0
	s_load_dwordx2 s[38:39], s[2:3], 0x90
	s_load_dwordx2 s[40:41], s[2:3], 0x98
	s_load_dwordx2 s[34:35], s[2:3], 0xa0
	s_lshl_b32 s0, s0, 3
	s_add_i32 s0, s0, 0xfa00
	v_mov_b32_e32 v131, 0x700
	s_waitcnt lgkmcnt(0)
	s_add_u32 s4, s90, 0x30a13600
	s_addc_u32 s5, s91, 0
	v_writelane_b32 v250, s4, 6
	v_mov_b32_e32 v130, v0
	s_nop 0
	v_writelane_b32 v250, s5, 7
	s_add_u32 s4, s90, 0x46a13600
	s_addc_u32 s5, s91, 0
	v_writelane_b32 v250, s4, 8
	v_ashrrev_i32_e32 v2, 6, v130
	v_add_u32_e32 v5, s0, v2
	v_writelane_b32 v250, s5, 9
	s_mov_b32 s4, 0x10800
	v_cmp_gt_i32_e32 vcc, s4, v5
	s_and_saveexec_b64 s[4:5], vcc
	s_cbranch_execz .Lcvp14_62
	s_movk_i32 s6, 0x4100
	v_mul_lo_u32 v3, v2, s6
	v_add_u32_e32 v8, 0, v3
	v_lshlrev_b32_e32 v3, 2, v130
	v_bfe_u32 v6, v130, 4, 2
	v_and_b32_e32 v44, 60, v3
	v_bfe_u32 v7, v130, 3, 3
	v_lshlrev_b32_e32 v130, 3, v130
	v_lshl_add_u32 v20, v44, 2, v8
	v_mul_u32_u24_e32 v21, 0x104, v6
	v_and_b32_e32 v130, 56, v130
	v_mul_u32_u24_e32 v9, 0x104, v130
	v_lshlrev_b32_e32 v10, 2, v7
	v_lshlrev_b32_e32 v16, 2, v2
	v_add_u32_e32 v20, v20, v21
	v_mov_b32_e32 v3, 0
	v_add3_u32 v8, v8, v9, v10
	v_or_b32_e32 v9, 8, v7
	v_or_b32_e32 v10, 16, v7
	v_or_b32_e32 v11, 24, v7
	v_or_b32_e32 v12, 32, v7
	v_or_b32_e32 v13, 40, v7
	v_or_b32_e32 v14, 48, v7
	v_or_b32_e32 v15, 56, v7
	v_lshlrev_b32_e32 v16, 2, v5
	v_lshlrev_b32_e32 v17, 2, v131
	v_lshlrev_b32_e32 v18, 6, v5
	v_lshlrev_b32_e32 v19, 6, v131
	s_mov_b64 s[6:7], 0
	s_mov_b32 s3, 0x3e0f83e1
	s_movk_i32 s10, 0x57f
	s_mov_b32 s11, 0xb00000
	v_add_u32_e32 v21, 0x410, v20
	v_add_u32_e32 v22, 0x418, v20
	v_add_u32_e32 v23, 0x820, v20
	v_add_u32_e32 v24, 0x828, v20
	v_add_u32_e32 v25, 0xc30, v20
	v_add_u32_e32 v26, 0xc38, v20
	v_add_u32_e32 v27, 0x1040, v20
	v_add_u32_e32 v28, 0x1048, v20
	v_add_u32_e32 v29, 0x1450, v20
	v_add_u32_e32 v30, 0x1458, v20
	v_add_u32_e32 v31, 0x1860, v20
	v_add_u32_e32 v32, 0x1868, v20
	v_add_u32_e32 v33, 0x1c70, v20
	v_add_u32_e32 v34, 0x1c78, v20
	v_add_u32_e32 v35, 0x2080, v20
	v_add_u32_e32 v36, 0x2088, v20
	v_add_u32_e32 v37, 0x2490, v20
	v_add_u32_e32 v38, 0x2498, v20
	v_add_u32_e32 v39, 0x28a0, v20
	v_add_u32_e32 v40, 0x28a8, v20
	v_add_u32_e32 v41, 0x2cb0, v20
	v_add_u32_e32 v42, 0x2cb8, v20
	s_movk_i32 s64, 0xba3
	s_mov_b32 s65, 0xb000
	s_mov_b32 s66, 0x16000
	s_mov_b32 s67, 0x21000
	s_mov_b32 s16, 0x2c000
	s_mov_b32 s68, 0x37000
	s_mov_b32 s69, 0x42000
	s_mov_b32 s19, 0x4d000
	s_mov_b32 s20, 0x58000
	s_mov_b32 s21, 0x63000
	s_mov_b32 s70, 0x6e000
	s_mov_b32 s23, 0x79000
	s_mov_b32 s24, 0x84000
	s_mov_b32 s25, 0x8f000
	s_mov_b32 s26, 0x9a000
	s_mov_b32 s27, 0xa5000
	s_mov_b32 s71, 0x107ff
	v_lshlrev_b32_e32 v2, 2, v44
	v_add_u32_e32 v43, 0x30c0, v20
	v_add_u32_e32 v44, 0x30c8, v20
	v_add_u32_e32 v45, 0x34d0, v20
	v_add_u32_e32 v46, 0x34d8, v20
	v_mov_b32_e32 v47, 6
	v_mov_b32_e32 v132, 1
	v_mov_b32_e32 v133, 8
	v_mov_b32_e32 v134, 7
	s_branch .Lcvp14_58

; __device__ __forceinline__ void xcd_barrier(const XcdBarrier& b) {
;     asm volatile("s_waitcnt vmcnt(0)" ::: "memory");
;     __syncthreads();
;     if (threadIdx.x == 0) {
;         unsigned* bar = b.bar;
;         __builtin_amdgcn_s_waitcnt(0);
;         unsigned nloc = b.st[0], nx = b.st[1];
;         if (nloc == 0u) { xcd_barrier_complete(bar, b.x, nloc, nx); b.st[0] = nloc; b.st[1] = nx; }
.Lcvp14_exit:
.LBB0_2271:
	s_waitcnt vmcnt(0)
	s_barrier
	s_mov_b64 s[0:1], exec
	v_readlane_b32 s2, v250, 0
	v_readlane_b32 s3, v250, 1
	s_and_b64 s[2:3], s[0:1], s[2:3]
	s_mov_b64 exec, s[2:3]
	s_cbranch_execz .LBB0_2323
	s_add_i32 s2, 0, 0x25ff0
	v_mov_b32_e32 v1, s2
	s_waitcnt vmcnt(0) expcnt(0) lgkmcnt(0)
	ds_read_b32 v3, v1
	s_add_i32 s2, 0, 0x25ff4
	v_mov_b32_e32 v1, s2
	ds_read_b32 v1, v1
	s_waitcnt lgkmcnt(1)
	v_cmp_ne_u32_e32 vcc, 0, v3
	s_cbranch_vccnz .LBB0_2287
	v_readlane_b32 s6, v250, 26
	v_readlane_b32 s7, v250, 27
	s_load_dword s4, s[6:7], 0x14
	s_load_dwordx2 s[2:3], s[6:7], 0x4
	s_mov_b32 s17, 1
	v_mov_b32_e32 v17, 0
	s_waitcnt lgkmcnt(0)
	s_lshr_b32 s6, s4, 16
	s_and_b32 s4, s4, 0xffff
	s_cmp_lg_u32 s4, 0
	s_cselect_b64 s[4:5], -1, 0
	s_cmp_lg_u64 s[4:5], 0
	s_addc_u32 s2, s2, 0
	s_cmp_lg_u32 s6, 0
	s_cselect_b64 s[4:5], -1, 0
	s_cmp_lg_u64 s[4:5], 0
	s_mul_i32 s16, s2, s33
	s_addc_u32 s2, s3, 0
	s_mul_i32 s16, s16, s2
	s_add_u32 s2, s90, 0x1000
	s_addc_u32 s3, s91, 0
	s_add_u32 s4, s90, 0x1100
	s_addc_u32 s5, s91, 0
	s_add_u32 s6, s90, 0x1200
	s_addc_u32 s7, s91, 0
	s_add_u32 s8, s90, 0x1300
	s_addc_u32 s9, s91, 0
	s_branch .LBB0_2275
